# RWKV prep: previous-token r/k/v pieces taken from the neighbouring lane (DPP), only the tile's first token fetches them
# speedup vs baseline: 1.0093x; 1.0085x over previous
; DI void phase_rwkvprep(const Args& a, int l, LAS unsigned char* lds, int tid, int gw, int NGW, int lane) {
;     ...
;         const int hd = u & 15, tile = u >> 4; const int b = tile / (L / 16), t0 = (tile % (L / 16)) * 16; const int row = b * L + t0 + tk, t = t0 + tk;
;         const bf16* zrow = Z + (size_t)row * NZ; const bf16* prow = zrow - NZ; const bool hp = t > 0;
;         const bf16* zc = zrow + ZR0; const bf16* zp = prow + ZR0;
;         struct CtIn { bf16x8 wd[2], wi[2], wg[2], wv; u32x2 zr, zk, zv, pr, pk, pv, vf; };
.LBB0_858:
	s_ashr_i32 s13, s24, 4
	s_mul_hi_i32 s1, s13, 0xfe03f81
	s_lshr_b32 s2, s1, 31
	s_ashr_i32 s1, s1, 3
	s_add_i32 s1, s1, s2
	s_mul_i32 s2, s1, 0x81
	s_sub_i32 s2, s13, s2
	s_lshl_b32 s4, s2, 4
	s_mulk_i32 s1, 0x810
	s_add_i32 s1, s1, s4
	v_or_b32_e32 v140, s1, v129
	v_mov_b64_e32 v[58:59], s[56:57]
	v_mad_i64_i32 v[120:121], s[2:3], v140, s15, v[58:59]
	s_mov_b64 s[2:3], 0x2c00
	s_nop 0
	v_lshl_add_u64 v[122:123], v[120:121], 0, s[2:3]
	v_or_b32_e32 v197, s25, v194
	s_mov_b64 s[2:3], 0x3400
	v_lshlrev_b32_e32 v90, 1, v197
	v_lshl_add_u64 v[126:127], v[120:121], 0, s[2:3]
	s_mov_b64 s[2:3], 0x3c00
	v_lshl_add_u64 v[58:59], v[122:123], 0, v[90:91]
	v_lshl_add_u64 v[142:143], v[120:121], 0, s[2:3]
	v_lshl_add_u64 v[60:61], v[126:127], 0, v[90:91]
	v_lshl_add_u64 v[62:63], v[142:143], 0, v[90:91]
	global_load_dwordx2 v[114:115], v[58:59], off
	global_load_dwordx2 v[112:113], v[60:61], off
	global_load_dwordx2 v[148:149], v[62:63], off
	s_movk_i32 s2, 0xe600
	v_or_b32_e32 v58, s4, v129
	s_mov_b32 s3, -1
	v_mov_b32_e32 v146, 0
	v_cmp_lt_i32_e64 s[46:47], 0, v58
	s_mov_b32 s82, 0x10001
	s_and_b32 s80, s46, s82
	s_and_b32 s81, s47, s82
	v_lshl_add_u64 v[124:125], v[120:121], 0, s[2:3]
	v_mov_b32_e32 v116, 0
	v_mov_b32_e32 v117, 0
	v_mov_b32_e32 v118, 0
	v_mov_b32_e32 v119, 0
	v_mov_b32_e32 v150, 0
	v_mov_b32_e32 v151, 0
	s_and_saveexec_b64 s[2:3], s[80:81]
	s_cbranch_execz .LBB0_860
	v_lshl_add_u64 v[60:61], v[120:121], 0, v[90:91]
	v_lshl_add_u64 v[58:59], v[124:125], 0, v[90:91]
	v_add_co_u32_e32 v62, vcc, 0xfffff000, v60
	s_nop 1
	v_addc_co_u32_e32 v63, vcc, -1, v61, vcc
	global_load_dwordx2 v[116:117], v[58:59], off
	global_load_dwordx2 v[118:119], v[62:63], off offset:-512
	global_load_dwordx2 v[150:151], v[60:61], off offset:-2560

.LBB0_882:
	v_or_b32_e32 v86, s0, v194
	v_lshlrev_b32_e32 v90, 1, v86
	v_lshl_add_u64 v[86:87], v[122:123], 0, v[90:91]
	v_lshl_add_u64 v[88:89], v[126:127], 0, v[90:91]
	v_lshl_add_u64 v[92:93], v[142:143], 0, v[90:91]
	global_load_dwordx2 v[160:161], v[86:87], off
	global_load_dwordx2 v[156:157], v[88:89], off
	global_load_dwordx2 v[182:183], v[92:93], off
	s_movk_i32 s0, 0xee00
	s_mov_b32 s1, -1
	v_lshl_add_u64 v[158:159], v[120:121], 0, s[0:1]
	v_mov_b32_e32 v154, 0
	v_mov_b32_e32 v174, 0
	v_mov_b32_e32 v175, 0
	v_mov_b32_e32 v176, 0
	v_mov_b32_e32 v177, 0
	v_mov_b32_e32 v188, 0
	v_mov_b32_e32 v189, 0
	s_and_saveexec_b64 s[2:3], s[80:81]
	s_cbranch_execz .LBB0_884
	v_lshl_add_u64 v[86:87], v[124:125], 0, v[90:91]
	v_lshl_add_u64 v[88:89], v[158:159], 0, v[90:91]
	v_add_lshl_u32 v90, s25, v194, 1
	v_lshl_add_u64 v[92:93], v[120:121], 0, v[90:91]
	global_load_dwordx2 v[174:175], v[86:87], off
	global_load_dwordx2 v[176:177], v[88:89], off
	global_load_dwordx2 v[188:189], v[92:93], off offset:-2528

; #define LAS __attribute__((address_space(3)))
; DI void phase_rwkvprep(const Args& a, int l, LAS unsigned char* lds, int tid, int gw, int NGW, int lane) {
;     ...
;             const u32x2 zr_ = I.zr, zk_ = I.zk, zv_ = I.zv, pr_ = I.pr, pk_ = I.pk, pv_ = I.pv, vfw = I.vf;
;             const f32x4 mr = *(const LAS f32x4*)(par + c0), mk = *(const LAS f32x4*)(par + C + c0), mv = *(const LAS f32x4*)(par + 2 * C + c0);
;             const f32x4 w0v = *(const LAS f32x4*)(par + 3 * C + c0), a0v = *(const LAS f32x4*)(par + 4 * C + c0), kkw = *(const LAS f32x4*)(par + 5 * C + c0), kaw = *(const LAS f32x4*)(par + 6 * C + c0), rkw = *(const LAS f32x4*)(par + 7 * C + c0);
;             const f32x4 v0v = *(const LAS f32x4*)(par + 8 * C + c0);
;             f32x4 ro, wo, ko, vo, go;
; #pragma unroll
;             for (int j = 0; j < 4; ++j) {
;                 const float rc = (j & 1) ? bfhi(j < 2 ? zr_.x : zr_.y) : bflo(j < 2 ? zr_.x : zr_.y), rp = (j & 1) ? bfhi(j < 2 ? pr_.x : pr_.y) : bflo(j < 2 ? pr_.x : pr_.y);
;                 const float kc = (j & 1) ? bfhi(j < 2 ? zk_.x : zk_.y) : bflo(j < 2 ? zk_.x : zk_.y), kp = (j & 1) ? bfhi(j < 2 ? pk_.x : pk_.y) : bflo(j < 2 ? pk_.x : pk_.y);
;                 const float vc = (j & 1) ? bfhi(j < 2 ? zv_.x : zv_.y) : bflo(j < 2 ? zv_.x : zv_.y), vp = (j & 1) ? bfhi(j < 2 ? pv_.x : pv_.y) : bflo(j < 2 ? pv_.x : pv_.y);
;                 const float vfj = (j & 1) ? bfhi(j < 2 ? vfw.x : vfw.y) : bflo(j < 2 ? vfw.x : vfw.y);
;                 const float r = rc + (rp - rc) * mr[j]; float k = kc + (kp - kc) * mk[j]; float v = vc + (vp - vc) * mv[j];
.LBB0_888:
	s_waitcnt vmcnt(9)
	v_mov_b32_dpp v116, v114 row_shr:1 row_mask:0xf bank_mask:0xf
	v_mov_b32_dpp v117, v115 row_shr:1 row_mask:0xf bank_mask:0xf
	v_mov_b32_dpp v118, v112 row_shr:1 row_mask:0xf bank_mask:0xf
	v_mov_b32_dpp v119, v113 row_shr:1 row_mask:0xf bank_mask:0xf
	v_mov_b32_dpp v150, v148 row_shr:1 row_mask:0xf bank_mask:0xf
	v_mov_b32_dpp v151, v149 row_shr:1 row_mask:0xf bank_mask:0xf
	v_lshlrev_b32_e32 v139, 16, v150
	v_lshlrev_b32_e32 v90, 16, v148
	v_lshl_add_u32 v209, v197, 2, 0
	v_sub_f32_e32 v139, v139, v90
	ds_read_b128 v[92:95], v209 offset:4096
	ds_read_b128 v[104:107], v209 offset:8192
	ds_read_b128 v[86:89], v209 offset:12288
	ds_read_b128 v[50:53], v209 offset:16384
	ds_read_b128 v[34:37], v209 offset:20480
	ds_read_b128 v[42:45], v209 offset:24576
	ds_read_b128 v[30:33], v209 offset:28672
	ds_read_b128 v[96:99], v209
	ds_read_b128 v[108:111], v209 offset:32768
	s_and_b64 vcc, exec, s[38:39]
	s_waitcnt lgkmcnt(7)
	v_fmac_f32_e32 v90, v139, v104
	s_cbranch_vccnz .LBB0_890
	s_waitcnt lgkmcnt(0)
	v_add_f32_e32 v100, v100, v108
	v_mul_f32_e32 v100, 0xbfb8aa3b, v100
	v_exp_f32_e32 v100, v100
	v_lshlrev_b32_e32 v104, 16, v146
	v_sub_f32_e32 v104, v104, v90
	v_add_f32_e32 v100, 1.0, v100
	v_rcp_f32_e32 v100, v100
	s_nop 0
	v_fmac_f32_e32 v90, v104, v100

.LBB0_901:
	v_or_b32_e32 v38, s0, v194
	v_lshlrev_b32_e32 v90, 1, v38
	v_lshl_add_u64 v[38:39], v[122:123], 0, v[90:91]
	v_lshl_add_u64 v[40:41], v[126:127], 0, v[90:91]
	v_lshl_add_u64 v[42:43], v[142:143], 0, v[90:91]
	global_load_dwordx2 v[172:173], v[38:39], off
	global_load_dwordx2 v[162:163], v[40:41], off
	global_load_dwordx2 v[186:187], v[42:43], off
	v_mov_b32_e32 v184, 0
	v_mov_b32_e32 v178, 0
	v_mov_b32_e32 v179, 0
	v_mov_b32_e32 v180, 0
	v_mov_b32_e32 v181, 0
	v_mov_b32_e32 v190, 0
	v_mov_b32_e32 v191, 0
	s_and_saveexec_b64 s[2:3], s[80:81]
	s_cbranch_execz .LBB0_903
	v_lshl_add_u64 v[38:39], v[124:125], 0, v[90:91]
	v_lshl_add_u64 v[40:41], v[158:159], 0, v[90:91]
	v_add_lshl_u32 v90, s25, v194, 1
	v_lshl_add_u64 v[42:43], v[120:121], 0, v[90:91]
	global_load_dwordx2 v[178:179], v[38:39], off
	global_load_dwordx2 v[180:181], v[40:41], off
	global_load_dwordx2 v[190:191], v[42:43], off offset:-2496

; #define LAS __attribute__((address_space(3)))
; DI void phase_rwkvprep(const Args& a, int l, LAS unsigned char* lds, int tid, int gw, int NGW, int lane) {
;     ...
;             const u32x2 zr_ = I.zr, zk_ = I.zk, zv_ = I.zv, pr_ = I.pr, pk_ = I.pk, pv_ = I.pv, vfw = I.vf;
;             const f32x4 mr = *(const LAS f32x4*)(par + c0), mk = *(const LAS f32x4*)(par + C + c0), mv = *(const LAS f32x4*)(par + 2 * C + c0);
;             const f32x4 w0v = *(const LAS f32x4*)(par + 3 * C + c0), a0v = *(const LAS f32x4*)(par + 4 * C + c0), kkw = *(const LAS f32x4*)(par + 5 * C + c0), kaw = *(const LAS f32x4*)(par + 6 * C + c0), rkw = *(const LAS f32x4*)(par + 7 * C + c0);
;             const f32x4 v0v = *(const LAS f32x4*)(par + 8 * C + c0);
;             f32x4 ro, wo, ko, vo, go;
; #pragma unroll
;             for (int j = 0; j < 4; ++j) {
;                 const float rc = (j & 1) ? bfhi(j < 2 ? zr_.x : zr_.y) : bflo(j < 2 ? zr_.x : zr_.y), rp = (j & 1) ? bfhi(j < 2 ? pr_.x : pr_.y) : bflo(j < 2 ? pr_.x : pr_.y);
;                 const float kc = (j & 1) ? bfhi(j < 2 ? zk_.x : zk_.y) : bflo(j < 2 ? zk_.x : zk_.y), kp = (j & 1) ? bfhi(j < 2 ? pk_.x : pk_.y) : bflo(j < 2 ? pk_.x : pk_.y);
;                 const float vc = (j & 1) ? bfhi(j < 2 ? zv_.x : zv_.y) : bflo(j < 2 ? zv_.x : zv_.y), vp = (j & 1) ? bfhi(j < 2 ? pv_.x : pv_.y) : bflo(j < 2 ? pv_.x : pv_.y);
;                 const float vfj = (j & 1) ? bfhi(j < 2 ? vfw.x : vfw.y) : bflo(j < 2 ? vfw.x : vfw.y);
;                 const float r = rc + (rp - rc) * mr[j]; float k = kc + (kp - kc) * mk[j]; float v = vc + (vp - vc) * mv[j];
.LBB0_907:
	s_waitcnt vmcnt(14)
	v_mov_b32_dpp v174, v160 row_shr:1 row_mask:0xf bank_mask:0xf
	v_mov_b32_dpp v175, v161 row_shr:1 row_mask:0xf bank_mask:0xf
	v_mov_b32_dpp v176, v156 row_shr:1 row_mask:0xf bank_mask:0xf
	v_mov_b32_dpp v177, v157 row_shr:1 row_mask:0xf bank_mask:0xf
	v_mov_b32_dpp v188, v182 row_shr:1 row_mask:0xf bank_mask:0xf
	v_mov_b32_dpp v189, v183 row_shr:1 row_mask:0xf bank_mask:0xf
	v_lshlrev_b32_e32 v164, 16, v188
	v_lshlrev_b32_e32 v90, 16, v182
	v_sub_f32_e32 v164, v164, v90
	ds_read_b128 v[82:85], v209 offset:4160
	ds_read_b128 v[112:115], v209 offset:8256
	ds_read_b128 v[78:81], v209 offset:12352
	ds_read_b128 v[70:73], v209 offset:16448
	ds_read_b128 v[42:45], v209 offset:20544
	ds_read_b128 v[62:65], v209 offset:24640
	ds_read_b128 v[38:41], v209 offset:28736
	ds_read_b128 v[104:107], v209 offset:64
	ds_read_b128 v[116:119], v209 offset:32832
	s_and_b64 vcc, exec, s[38:39]
	s_waitcnt lgkmcnt(7)
	v_fmac_f32_e32 v90, v164, v112
	s_cbranch_vccnz .LBB0_909
	s_waitcnt lgkmcnt(0)
	v_add_f32_e32 v108, v108, v116
	v_mul_f32_e32 v108, 0xbfb8aa3b, v108
	v_exp_f32_e32 v108, v108
	v_lshlrev_b32_e32 v112, 16, v154
	v_sub_f32_e32 v112, v112, v90
	v_add_f32_e32 v108, 1.0, v108
	v_rcp_f32_e32 v108, v108
	s_nop 0
	v_fmac_f32_e32 v90, v112, v108

.LBB0_920:
	v_or_b32_e32 v90, s0, v194
	v_lshlrev_b32_e32 v90, 1, v90
	v_lshl_add_u64 v[104:105], v[122:123], 0, v[90:91]
	v_lshl_add_u64 v[106:107], v[126:127], 0, v[90:91]
	v_lshl_add_u64 v[108:109], v[142:143], 0, v[90:91]
	global_load_dwordx2 v[160:161], v[104:105], off
	global_load_dwordx2 v[142:143], v[106:107], off
	global_load_dwordx2 v[188:189], v[108:109], off
	v_mov_b32_e32 v182, 0
	v_mov_b32_e32 v174, 0
	v_mov_b32_e32 v175, 0
	v_mov_b32_e32 v176, 0
	v_mov_b32_e32 v177, 0
	v_mov_b32_e32 v192, 0
	v_mov_b32_e32 v193, 0
	s_and_saveexec_b64 s[2:3], s[80:81]
	s_cbranch_execz .LBB0_922
	v_lshl_add_u64 v[104:105], v[124:125], 0, v[90:91]
	v_lshl_add_u64 v[106:107], v[158:159], 0, v[90:91]
	v_add_lshl_u32 v90, s25, v194, 1
	v_lshl_add_u64 v[108:109], v[120:121], 0, v[90:91]
	global_load_dwordx2 v[174:175], v[104:105], off
	global_load_dwordx2 v[176:177], v[106:107], off
	global_load_dwordx2 v[192:193], v[108:109], off offset:-2464

; #define LAS __attribute__((address_space(3)))
; DI void phase_rwkvprep(const Args& a, int l, LAS unsigned char* lds, int tid, int gw, int NGW, int lane) {
;     ...
;             const u32x2 zr_ = I.zr, zk_ = I.zk, zv_ = I.zv, pr_ = I.pr, pk_ = I.pk, pv_ = I.pv, vfw = I.vf;
;             const f32x4 mr = *(const LAS f32x4*)(par + c0), mk = *(const LAS f32x4*)(par + C + c0), mv = *(const LAS f32x4*)(par + 2 * C + c0);
;             const f32x4 w0v = *(const LAS f32x4*)(par + 3 * C + c0), a0v = *(const LAS f32x4*)(par + 4 * C + c0), kkw = *(const LAS f32x4*)(par + 5 * C + c0), kaw = *(const LAS f32x4*)(par + 6 * C + c0), rkw = *(const LAS f32x4*)(par + 7 * C + c0);
;             const f32x4 v0v = *(const LAS f32x4*)(par + 8 * C + c0);
;             f32x4 ro, wo, ko, vo, go;
; #pragma unroll
;             for (int j = 0; j < 4; ++j) {
;                 const float rc = (j & 1) ? bfhi(j < 2 ? zr_.x : zr_.y) : bflo(j < 2 ? zr_.x : zr_.y), rp = (j & 1) ? bfhi(j < 2 ? pr_.x : pr_.y) : bflo(j < 2 ? pr_.x : pr_.y);
;                 const float kc = (j & 1) ? bfhi(j < 2 ? zk_.x : zk_.y) : bflo(j < 2 ? zk_.x : zk_.y), kp = (j & 1) ? bfhi(j < 2 ? pk_.x : pk_.y) : bflo(j < 2 ? pk_.x : pk_.y);
;                 const float vc = (j & 1) ? bfhi(j < 2 ? zv_.x : zv_.y) : bflo(j < 2 ? zv_.x : zv_.y), vp = (j & 1) ? bfhi(j < 2 ? pv_.x : pv_.y) : bflo(j < 2 ? pv_.x : pv_.y);
;                 const float vfj = (j & 1) ? bfhi(j < 2 ? vfw.x : vfw.y) : bflo(j < 2 ? vfw.x : vfw.y);
;                 const float r = rc + (rp - rc) * mr[j]; float k = kc + (kp - kc) * mk[j]; float v = vc + (vp - vc) * mv[j];
.LBB0_926:
	s_waitcnt vmcnt(14)
	v_mov_b32_dpp v178, v172 row_shr:1 row_mask:0xf bank_mask:0xf
	v_mov_b32_dpp v179, v173 row_shr:1 row_mask:0xf bank_mask:0xf
	v_mov_b32_dpp v180, v162 row_shr:1 row_mask:0xf bank_mask:0xf
	v_mov_b32_dpp v181, v163 row_shr:1 row_mask:0xf bank_mask:0xf
	v_mov_b32_dpp v190, v186 row_shr:1 row_mask:0xf bank_mask:0xf
	v_mov_b32_dpp v191, v187 row_shr:1 row_mask:0xf bank_mask:0xf
	v_lshlrev_b32_e32 v90, 16, v190
	v_lshlrev_b32_e32 v144, 16, v186
	v_sub_f32_e32 v90, v90, v144
	ds_read_b128 v[108:111], v209 offset:4224
	ds_read_b128 v[120:123], v209 offset:8320
	ds_read_b128 v[104:107], v209 offset:12416
	ds_read_b128 v[96:99], v209 offset:16512
	ds_read_b128 v[50:53], v209 offset:20608
	ds_read_b128 v[86:89], v209 offset:24704
	ds_read_b128 v[46:49], v209 offset:28800
	ds_read_b128 v[112:115], v209 offset:128
	ds_read_b128 v[124:127], v209 offset:32896
	s_and_b64 vcc, exec, s[38:39]
	s_waitcnt lgkmcnt(7)
	v_fmac_f32_e32 v144, v90, v120
	s_cbranch_vccnz .LBB0_928
	s_waitcnt lgkmcnt(0)
	v_add_f32_e32 v90, v116, v124
	v_mul_f32_e32 v90, 0xbfb8aa3b, v90
	v_exp_f32_e32 v90, v90
	v_lshlrev_b32_e32 v116, 16, v184
	v_sub_f32_e32 v116, v116, v144
	v_add_f32_e32 v90, 1.0, v90
	v_rcp_f32_e32 v90, v90
	s_nop 0
	v_fmac_f32_e32 v144, v116, v90

; #define LAS __attribute__((address_space(3)))
; DI float sigmoidf_(float x) { return 1.f / (1.f + __expf(-x)); }
; DI void phase_rwkvprep(const Args& a, int l, LAS unsigned char* lds, int tid, int gw, int NGW, int lane) {
;     ...
;             const u32x2 zr_ = I.zr, zk_ = I.zk, zv_ = I.zv, pr_ = I.pr, pk_ = I.pk, pv_ = I.pv, vfw = I.vf;
;             const f32x4 mr = *(const LAS f32x4*)(par + c0), mk = *(const LAS f32x4*)(par + C + c0), mv = *(const LAS f32x4*)(par + 2 * C + c0);
;             const f32x4 w0v = *(const LAS f32x4*)(par + 3 * C + c0), a0v = *(const LAS f32x4*)(par + 4 * C + c0), kkw = *(const LAS f32x4*)(par + 5 * C + c0), kaw = *(const LAS f32x4*)(par + 6 * C + c0), rkw = *(const LAS f32x4*)(par + 7 * C + c0);
;             const f32x4 v0v = *(const LAS f32x4*)(par + 8 * C + c0);
;             f32x4 ro, wo, ko, vo, go;
; #pragma unroll
;             for (int j = 0; j < 4; ++j) {
;                 const float rc = (j & 1) ? bfhi(j < 2 ? zr_.x : zr_.y) : bflo(j < 2 ? zr_.x : zr_.y), rp = (j & 1) ? bfhi(j < 2 ? pr_.x : pr_.y) : bflo(j < 2 ? pr_.x : pr_.y);
;                 const float kc = (j & 1) ? bfhi(j < 2 ? zk_.x : zk_.y) : bflo(j < 2 ? zk_.x : zk_.y), kp = (j & 1) ? bfhi(j < 2 ? pk_.x : pk_.y) : bflo(j < 2 ? pk_.x : pk_.y);
;                 const float vc = (j & 1) ? bfhi(j < 2 ? zv_.x : zv_.y) : bflo(j < 2 ? zv_.x : zv_.y), vp = (j & 1) ? bfhi(j < 2 ? pv_.x : pv_.y) : bflo(j < 2 ? pv_.x : pv_.y);
;                 const float vfj = (j & 1) ? bfhi(j < 2 ? vfw.x : vfw.y) : bflo(j < 2 ? vfw.x : vfw.y);
;                 const float r = rc + (rp - rc) * mr[j]; float k = kc + (kp - kc) * mk[j]; float v = vc + (vp - vc) * mv[j];
;                 const float xw = -(w0v[j] + aw[j]);
;                 const float sp = fmaxf(xw, 0.f) + __logf(1.f + __expf(-fabsf(xw)));
;                 const float wlog = -sp - 0.5f; const float dec = __expf(-__expf(wlog));
;                 const float aval = sigmoidf_(a0v[j] + aa[j]);
;                 if (l > 0) v = v + (vfj - v) * sigmoidf_(v0v[j] + avr[j]);
.LBB0_938:
	s_waitcnt vmcnt(5)
	v_mov_b32_dpp v174, v160 row_shr:1 row_mask:0xf bank_mask:0xf
	v_mov_b32_dpp v175, v161 row_shr:1 row_mask:0xf bank_mask:0xf
	v_mov_b32_dpp v176, v142 row_shr:1 row_mask:0xf bank_mask:0xf
	v_mov_b32_dpp v177, v143 row_shr:1 row_mask:0xf bank_mask:0xf
	v_mov_b32_dpp v192, v188 row_shr:1 row_mask:0xf bank_mask:0xf
	v_mov_b32_dpp v193, v189 row_shr:1 row_mask:0xf bank_mask:0xf
	v_lshlrev_b32_e32 v124, 16, v192
	v_lshlrev_b32_e32 v123, 16, v188
	v_sub_f32_e32 v124, v124, v123
	ds_read_b128 v[86:89], v209 offset:4288
	ds_read_b128 v[100:103], v209 offset:8384
	ds_read_b128 v[82:85], v209 offset:12480
	ds_read_b128 v[74:77], v209 offset:16576
	ds_read_b128 v[58:61], v209 offset:20672
	ds_read_b128 v[62:65], v209 offset:24768
	ds_read_b128 v[54:57], v209 offset:28864
	ds_read_b128 v[92:95], v209 offset:192
	ds_read_b128 v[104:107], v209 offset:32960
	s_and_b64 vcc, exec, s[38:39]
	s_waitcnt lgkmcnt(7)
	v_fmac_f32_e32 v123, v124, v100
	s_cbranch_vccnz .LBB0_940
	s_waitcnt lgkmcnt(0)
	v_add_f32_e32 v96, v96, v104
	v_mul_f32_e32 v96, 0xbfb8aa3b, v96
	v_exp_f32_e32 v96, v96
	v_lshlrev_b32_e32 v100, 16, v182
	v_sub_f32_e32 v100, v100, v123
	v_add_f32_e32 v96, 1.0, v96
	v_rcp_f32_e32 v96, v96
	s_nop 0
	v_fmac_f32_e32 v123, v100, v96
